# gemm1 loops: DMA address VALU in the pre-barrier tail (v47) combined with one static s_setprio 1 for waves 4-7 in the QKV loop (v48)
# baseline (speedup 1.0000x reference)
.Lqk_bias_done:
	v_lshlrev_b32_e32 v5, 7, v0
	v_lshlrev_b32_e32 v2, 3, v2
	s_mov_b32 s7, 0x1fc00
	v_mov_b32_e32 v6, 0x10000
	s_add_u32 s16, s24, s18
	v_and_b32_e32 v3, 56, v2
	v_and_b32_e32 v4, 0xfc00, v5
	v_bitop3_b32 v5, v5, s7, v6 bitop3:0xc8
	v_lshlrev_b32_e32 v8, 8, v0
	s_mov_b32 s7, 0x3f800
	v_mov_b32_e32 v7, 0x20000
	s_addc_u32 s17, s25, s19
	v_or_b32_e32 v2, v4, v3
	v_bitop3_b32 v7, v8, s7, v7 bitop3:0xc8
	s_mov_b32 s7, 0x7f800
	v_mov_b32_e32 v11, 0x60000
	s_waitcnt lgkmcnt(0)
	s_add_u32 s22, s0, s2
	v_and_b32_e32 v6, 0x1f800, v8
	v_bitop3_b32 v8, v8, s7, v11 bitop3:0xc8
	v_lshlrev_b32_e32 v12, 1, v2
	v_mov_b32_e32 v2, 0
	v_readfirstlane_b32 s7, v79
	v_or_b32_e32 v9, v5, v3
	s_addc_u32 s23, s1, s3
	v_mov_b32_e32 v13, v2
	s_mov_b32 m0, s7
	v_lshl_add_u64 v[14:15], s[22:23], 0, v[12:13]
	global_load_lds_dwordx4 v12, s[22:23]
	v_lshlrev_b32_e32 v12, 1, v9
	v_or_b32_e32 v9, 0x2000, v79
	v_or_b32_e32 v10, v6, v3
	v_readfirstlane_b32 s7, v9
	v_or_b32_e32 v9, 0x4000, v79
	s_mov_b32 m0, s7
	v_readfirstlane_b32 s7, v9
	v_or_b32_e32 v9, 0x6000, v79
	v_or_b32_e32 v18, v7, v3
	v_lshlrev_b32_e32 v10, 1, v10
	global_load_lds_dwordx4 v12, s[22:23]
	s_mov_b32 m0, s7
	v_readfirstlane_b32 s7, v9
	v_or_b32_e32 v9, 0x8000, v79
	v_mov_b32_e32 v11, v2
	global_load_lds_dwordx4 v10, s[16:17]
	v_lshlrev_b32_e32 v18, 1, v18
	s_mov_b32 m0, s7
	v_readfirstlane_b32 s7, v9
	v_or_b32_e32 v9, 0xa000, v79
	v_or_b32_e32 v22, v8, v3
	v_lshl_add_u64 v[16:17], s[22:23], 0, v[12:13]
	v_lshl_add_u64 v[12:13], s[16:17], 0, v[10:11]
	v_mov_b32_e32 v19, v2
	global_load_lds_dwordx4 v18, s[16:17]
	v_or_b32_e32 v10, 0x80000, v10
	s_mov_b32 m0, s7
	v_readfirstlane_b32 s7, v9
	v_lshl_add_u64 v[20:21], s[16:17], 0, v[18:19]
	v_lshl_add_u64 v[18:19], s[16:17], 0, v[10:11]
	global_load_lds_dwordx4 v10, s[16:17]
	v_lshlrev_b32_e32 v10, 1, v22
	s_mov_b32 m0, s7
	v_or_b32_e32 v9, 0xc000, v79
	v_lshl_add_u64 v[22:23], s[16:17], 0, v[10:11]
	global_load_lds_dwordx4 v10, s[16:17]
	s_mov_b64 s[16:17], 0x80
	v_readfirstlane_b32 s7, v9
	v_or_b32_e32 v9, 0xe000, v79
	v_lshl_add_u64 v[10:11], v[14:15], 0, s[16:17]
	s_mov_b32 m0, s7
	v_readfirstlane_b32 s7, v9
	v_or_b32_e32 v9, 0x10000, v79
	global_load_lds_dwordx4 v[10:11], off
	v_lshl_add_u64 v[10:11], v[16:17], 0, s[16:17]
	s_mov_b32 m0, s7
	v_readfirstlane_b32 s7, v9
	v_or_b32_e32 v9, 0x12000, v79
	global_load_lds_dwordx4 v[10:11], off
	v_lshl_add_u64 v[10:11], v[12:13], 0, s[16:17]
	s_mov_b32 m0, s7
	v_readfirstlane_b32 s7, v9
	v_or_b32_e32 v9, 0x14000, v79
	global_load_lds_dwordx4 v[10:11], off
	v_lshl_add_u64 v[10:11], v[20:21], 0, s[16:17]
	s_mov_b32 m0, s7
	v_readfirstlane_b32 s7, v9
	v_or_b32_e32 v9, 0x16000, v79
	global_load_lds_dwordx4 v[10:11], off
	v_lshl_add_u64 v[10:11], v[18:19], 0, s[16:17]
	s_mov_b32 m0, s7
	v_readfirstlane_b32 s7, v9
	global_load_lds_dwordx4 v[10:11], off
	v_lshl_add_u64 v[10:11], v[22:23], 0, s[16:17]
	s_mov_b32 m0, s7
	s_nop 0
	global_load_lds_dwordx4 v[10:11], off
	s_cmp_lt_i32 s20, 16
	s_cselect_b64 s[16:17], -1, 0
	s_cmp_gt_i32 s20, 15
	v_bfe_u32 v9, v0, 6, 2
	s_cselect_b64 vcc, -1, 0
	v_cndmask_b32_e32 v83, v78, v9, vcc
	v_cndmask_b32_e32 v9, v9, v78, vcc
	s_and_b64 s[22:23], vcc, exec
	v_lshl_or_b32 v80, v9, 6, v42
	v_bfe_u32 v9, v0, 1, 3
	s_cselect_b32 s26, 0x2000, 0
	s_cselect_b32 s27, 0, 0x2000
	v_bitop3_b32 v9, v1, v9, 4 bitop3:0x36
	s_add_u32 s18, s24, s18
	v_lshlrev_b32_e32 v84, 4, v9
	v_add_lshl_u32 v8, v8, v3, 1
	v_mov_b32_e32 v9, v2
	s_addc_u32 s19, s25, s19
	v_lshl_add_u64 v[8:9], s[18:19], 0, v[8:9]
	s_mov_b64 s[22:23], 0x100
	v_lshl_add_u64 v[66:67], v[8:9], 0, s[22:23]
	v_add_lshl_u32 v8, v7, v3, 1
	v_mov_b32_e32 v9, v2
	v_lshl_add_u64 v[8:9], s[18:19], 0, v[8:9]
	v_add_lshl_u32 v6, v6, v3, 1
	v_mov_b32_e32 v7, v2
	v_lshl_add_u64 v[68:69], v[8:9], 0, s[22:23]
	v_lshl_add_u64 v[8:9], s[18:19], 0, v[6:7]
	v_or_b32_e32 v6, 0x80000, v6
	v_lshlrev_b32_e32 v82, 6, v83
	v_lshl_add_u64 v[6:7], s[18:19], 0, v[6:7]
	s_add_u32 s0, s0, s2
	v_or_b32_e32 v10, v82, v42
	v_lshl_add_u64 v[72:73], v[6:7], 0, s[22:23]
	v_add_lshl_u32 v6, v5, v3, 1
	v_mov_b32_e32 v7, v2
	s_addc_u32 s1, s1, s3
	v_add_lshl_u32 v4, v4, v3, 1
	v_mov_b32_e32 v5, v2
	v_lshlrev_b32_e32 v86, 7, v10
	v_bitop3_b32 v10, v43, v1, 7 bitop3:0x6c
	v_lshl_add_u64 v[6:7], s[0:1], 0, v[6:7]
	v_lshl_add_u64 v[4:5], s[0:1], 0, v[4:5]
	v_lshlrev_b32_e32 v85, 4, v10
	v_lshlrev_b32_e32 v81, 7, v80
	v_lshl_add_u64 v[70:71], v[8:9], 0, s[22:23]
	v_lshl_add_u64 v[74:75], v[6:7], 0, s[22:23]
	v_lshl_add_u64 v[76:77], v[4:5], 0, s[22:23]
	s_mov_b32 s18, 2
	s_mov_b64 s[0:1], 0
	s_lshl_b32 s3, s26, 1
	s_lshl_b32 s2, s27, 1
	v_mov_b32_e32 v3, v2
	v_mov_b32_e32 v4, v2
	v_mov_b32_e32 v5, v2
	v_mov_b32_e32 v6, v2
	v_mov_b32_e32 v7, v2
	v_mov_b32_e32 v8, v2
	v_mov_b32_e32 v9, v2
	v_mov_b32_e32 v10, v2
	v_mov_b32_e32 v11, v2
	v_mov_b32_e32 v12, v2
	v_mov_b32_e32 v13, v2
	v_mov_b32_e32 v14, v2
	v_mov_b32_e32 v15, v2
	v_mov_b32_e32 v16, v2
	v_mov_b32_e32 v17, v2
	v_mov_b32_e32 v18, v2
	v_mov_b32_e32 v19, v2
	v_mov_b32_e32 v20, v2
	v_mov_b32_e32 v21, v2
	v_mov_b32_e32 v22, v2
	v_mov_b32_e32 v23, v2
	v_mov_b32_e32 v24, v2
	v_mov_b32_e32 v25, v2
	v_mov_b32_e32 v26, v2
	v_mov_b32_e32 v27, v2
	v_mov_b32_e32 v28, v2
	v_mov_b32_e32 v29, v2
	v_mov_b32_e32 v30, v2
	v_mov_b32_e32 v31, v2
	v_mov_b32_e32 v32, v2
	v_mov_b32_e32 v33, v2
	v_mov_b32_e32 v34, v2
	v_mov_b32_e32 v35, v2
	v_mov_b32_e32 v36, v2
	v_mov_b32_e32 v37, v2
	v_mov_b32_e32 v38, v2
	v_mov_b32_e32 v39, v2
	v_mov_b32_e32 v40, v2
	v_mov_b32_e32 v41, v2
	v_mov_b32_e32 v42, v2
	v_mov_b32_e32 v43, v2
	v_mov_b32_e32 v44, v2
	v_mov_b32_e32 v45, v2
	v_mov_b32_e32 v46, v2
	v_mov_b32_e32 v47, v2
	v_mov_b32_e32 v48, v2
	v_mov_b32_e32 v49, v2
	v_mov_b32_e32 v50, v2
	v_mov_b32_e32 v51, v2
	v_mov_b32_e32 v52, v2
	v_mov_b32_e32 v53, v2
	v_mov_b32_e32 v54, v2
	v_mov_b32_e32 v55, v2
	v_mov_b32_e32 v56, v2
	v_mov_b32_e32 v57, v2
	v_mov_b32_e32 v58, v2
	v_mov_b32_e32 v59, v2
	v_mov_b32_e32 v60, v2
	v_mov_b32_e32 v61, v2
	v_mov_b32_e32 v62, v2
	v_mov_b32_e32 v63, v2
	v_mov_b32_e32 v64, v2
	v_mov_b32_e32 v65, v2
	v_readfirstlane_b32 s44, v79
	s_mov_b32 s45, 0
	s_mov_b32 s46, 1
	s_mov_b32 s48, 0
	s_mov_b64 s[0:1], 0
	s_add_u32 s49, s44, 0x18000
	s_mov_b32 m0, s49
	s_nop 0
	global_load_lds_dwordx4 v[76:77], off
	s_add_u32 m0, s49, 0x2000
	s_nop 0
	global_load_lds_dwordx4 v[74:75], off
	s_add_u32 m0, s49, 0x4000
	s_nop 0
	global_load_lds_dwordx4 v[70:71], off
	s_add_u32 m0, s49, 0x6000
	s_nop 0
	global_load_lds_dwordx4 v[68:69], off
	s_add_u32 m0, s49, 0x8000
	s_nop 0
	global_load_lds_dwordx4 v[72:73], off
	s_add_u32 m0, s49, 0xa000
	s_nop 0
	global_load_lds_dwordx4 v[66:67], off
	s_mov_b64 s[0:1], 0x80
	v_lshl_add_u64 v[76:77], v[76:77], 0, s[0:1]
	v_lshl_add_u64 v[74:75], v[74:75], 0, s[0:1]
	v_lshl_add_u64 v[70:71], v[70:71], 0, s[0:1]
	v_lshl_add_u64 v[68:69], v[68:69], 0, s[0:1]
	v_lshl_add_u64 v[72:73], v[72:73], 0, s[0:1]
	v_lshl_add_u64 v[66:67], v[66:67], 0, s[0:1]
	s_waitcnt vmcnt(12)
	s_barrier
	s_mov_b32 s46, 0
	s_mul_i32 s49, s46, 0xc000
	s_add_u32 s50, s49, s3
	s_add_u32 s51, s49, s2
	v_add3_u32 v120, s50, v86, v85
	v_add3_u32 v121, s50, v86, v84
	v_add3_u32 v122, s51, v81, v85
	v_add3_u32 v123, s51, v81, v84
	ds_read_b128 v[88:91], v120
	ds_read_b128 v[92:95], v120 offset:2048
	ds_read_b128 v[96:99], v120 offset:4096
	ds_read_b128 v[100:103], v120 offset:6144
	ds_read_b128 v[104:107], v122
	ds_read_b128 v[108:111], v122 offset:2048
	ds_read_b128 v[112:115], v122 offset:4096
	ds_read_b128 v[116:119], v122 offset:6144
	ds_read_b128 v[144:147], v121
	ds_read_b128 v[148:151], v121 offset:2048
	ds_read_b128 v[152:155], v121 offset:4096
	ds_read_b128 v[156:159], v121 offset:6144
	ds_read_b128 v[160:163], v123
	ds_read_b128 v[164:167], v123 offset:2048
	ds_read_b128 v[168:171], v123 offset:4096
	ds_read_b128 v[172:175], v123 offset:6144
	s_mov_b32 s46, 1
	s_cmp_lt_u32 s44, 0x1000
	s_cbranch_scc1 .Lqk_prio_skip
	s_setprio 1
.Lqk_prio_skip:
.LBB1_36:
	s_waitcnt vmcnt(6)
	s_waitcnt lgkmcnt(0)
	s_barrier
	s_mul_i32 s49, s46, 0xc000
	s_add_u32 s50, s49, s3
	s_add_u32 s51, s49, s2
	v_add3_u32 v120, s50, v86, v85
	v_add3_u32 v121, s50, v86, v84
	v_add3_u32 v122, s51, v81, v85
	v_add3_u32 v123, s51, v81, v84
	s_mul_i32 s49, s45, 0xc000
	s_add_u32 s49, s49, s44
	ds_read_b128 v[176:179], v120
	ds_read_b128 v[180:183], v120 offset:2048
	ds_read_b128 v[184:187], v120 offset:4096
	ds_read_b128 v[188:191], v120 offset:6144
	v_mfma_f32_16x16x32_f16 v[62:65], v[88:91], v[104:107], v[62:65]
	ds_read_b128 v[192:195], v122
	v_mfma_f32_16x16x32_f16 v[58:61], v[88:91], v[108:111], v[58:61]
	ds_read_b128 v[196:199], v122 offset:2048
	v_mfma_f32_16x16x32_f16 v[54:57], v[88:91], v[112:115], v[54:57]
	ds_read_b128 v[200:203], v122 offset:4096
	v_mfma_f32_16x16x32_f16 v[50:53], v[88:91], v[116:119], v[50:53]
	ds_read_b128 v[204:207], v122 offset:6144
	v_mfma_f32_16x16x32_f16 v[46:49], v[92:95], v[104:107], v[46:49]
	ds_read_b128 v[208:211], v121
	v_mfma_f32_16x16x32_f16 v[42:45], v[92:95], v[108:111], v[42:45]
	ds_read_b128 v[212:215], v121 offset:2048
	v_mfma_f32_16x16x32_f16 v[38:41], v[92:95], v[112:115], v[38:41]
	ds_read_b128 v[216:219], v121 offset:4096
	v_mfma_f32_16x16x32_f16 v[34:37], v[92:95], v[116:119], v[34:37]
	ds_read_b128 v[220:223], v121 offset:6144
	v_mfma_f32_16x16x32_f16 v[30:33], v[96:99], v[104:107], v[30:33]
	ds_read_b128 v[224:227], v123
	v_mfma_f32_16x16x32_f16 v[26:29], v[96:99], v[108:111], v[26:29]
	ds_read_b128 v[228:231], v123 offset:2048
	v_mfma_f32_16x16x32_f16 v[22:25], v[96:99], v[112:115], v[22:25]
	ds_read_b128 v[232:235], v123 offset:4096
	v_mfma_f32_16x16x32_f16 v[18:21], v[96:99], v[116:119], v[18:21]
	ds_read_b128 v[236:239], v123 offset:6144
	v_mfma_f32_16x16x32_f16 v[14:17], v[100:103], v[104:107], v[14:17]
	v_mfma_f32_16x16x32_f16 v[10:13], v[100:103], v[108:111], v[10:13]
	s_mov_b32 m0, s49
	v_mfma_f32_16x16x32_f16 v[6:9], v[100:103], v[112:115], v[6:9]
	global_load_lds_dwordx4 v[76:77], off
	v_mfma_f32_16x16x32_f16 v[2:5], v[100:103], v[116:119], v[2:5]
	v_mfma_f32_16x16x32_f16 v[62:65], v[144:147], v[160:163], v[62:65]
	s_add_u32 m0, s49, 0x2000
	v_mfma_f32_16x16x32_f16 v[58:61], v[144:147], v[164:167], v[58:61]
	global_load_lds_dwordx4 v[74:75], off
	v_mfma_f32_16x16x32_f16 v[54:57], v[144:147], v[168:171], v[54:57]
	v_mfma_f32_16x16x32_f16 v[50:53], v[144:147], v[172:175], v[50:53]
	s_add_u32 m0, s49, 0x4000
	v_mfma_f32_16x16x32_f16 v[46:49], v[148:151], v[160:163], v[46:49]
	global_load_lds_dwordx4 v[70:71], off
	v_mfma_f32_16x16x32_f16 v[42:45], v[148:151], v[164:167], v[42:45]
	v_mfma_f32_16x16x32_f16 v[38:41], v[148:151], v[168:171], v[38:41]
	s_add_u32 m0, s49, 0x6000
	v_mfma_f32_16x16x32_f16 v[34:37], v[148:151], v[172:175], v[34:37]
	global_load_lds_dwordx4 v[68:69], off
	v_mfma_f32_16x16x32_f16 v[30:33], v[152:155], v[160:163], v[30:33]
	v_mfma_f32_16x16x32_f16 v[26:29], v[152:155], v[164:167], v[26:29]
	s_add_u32 m0, s49, 0x8000
	v_mfma_f32_16x16x32_f16 v[22:25], v[152:155], v[168:171], v[22:25]
	global_load_lds_dwordx4 v[72:73], off
	v_mfma_f32_16x16x32_f16 v[18:21], v[152:155], v[172:175], v[18:21]
	v_mfma_f32_16x16x32_f16 v[14:17], v[156:159], v[160:163], v[14:17]
	s_add_u32 m0, s49, 0xa000
	v_mfma_f32_16x16x32_f16 v[10:13], v[156:159], v[164:167], v[10:13]
	global_load_lds_dwordx4 v[66:67], off
	v_mfma_f32_16x16x32_f16 v[6:9], v[156:159], v[168:171], v[6:9]
	v_mfma_f32_16x16x32_f16 v[2:5], v[156:159], v[172:175], v[2:5]
	v_lshl_add_u64 v[76:77], v[76:77], 0, s[0:1]
	v_lshl_add_u64 v[74:75], v[74:75], 0, s[0:1]
	v_lshl_add_u64 v[70:71], v[70:71], 0, s[0:1]
	v_lshl_add_u64 v[68:69], v[68:69], 0, s[0:1]
	v_lshl_add_u64 v[72:73], v[72:73], 0, s[0:1]
	v_lshl_add_u64 v[66:67], v[66:67], 0, s[0:1]
	s_add_i32 s48, s48, 1
	s_add_i32 s49, s45, 1
	s_cmp_lg_u32 s45, 2
	s_cselect_b32 s45, s49, 0
	s_add_i32 s49, s46, 1
	s_cmp_lg_u32 s46, 2
	s_cselect_b32 s46, s49, 0
	s_waitcnt vmcnt(6)
	s_waitcnt lgkmcnt(0)
	s_barrier
	s_mul_i32 s49, s46, 0xc000
	s_add_u32 s50, s49, s3
	s_add_u32 s51, s49, s2
	v_add3_u32 v120, s50, v86, v85
	v_add3_u32 v121, s50, v86, v84
	v_add3_u32 v122, s51, v81, v85
	v_add3_u32 v123, s51, v81, v84
	s_mul_i32 s49, s45, 0xc000
	s_add_u32 s49, s49, s44
	ds_read_b128 v[88:91], v120
	ds_read_b128 v[92:95], v120 offset:2048
	ds_read_b128 v[96:99], v120 offset:4096
	ds_read_b128 v[100:103], v120 offset:6144
	v_mfma_f32_16x16x32_f16 v[62:65], v[176:179], v[192:195], v[62:65]
	ds_read_b128 v[104:107], v122
	v_mfma_f32_16x16x32_f16 v[58:61], v[176:179], v[196:199], v[58:61]
	ds_read_b128 v[108:111], v122 offset:2048
	v_mfma_f32_16x16x32_f16 v[54:57], v[176:179], v[200:203], v[54:57]
	ds_read_b128 v[112:115], v122 offset:4096
	v_mfma_f32_16x16x32_f16 v[50:53], v[176:179], v[204:207], v[50:53]
	ds_read_b128 v[116:119], v122 offset:6144
	v_mfma_f32_16x16x32_f16 v[46:49], v[180:183], v[192:195], v[46:49]
	ds_read_b128 v[144:147], v121
	v_mfma_f32_16x16x32_f16 v[42:45], v[180:183], v[196:199], v[42:45]
	ds_read_b128 v[148:151], v121 offset:2048
	v_mfma_f32_16x16x32_f16 v[38:41], v[180:183], v[200:203], v[38:41]
	ds_read_b128 v[152:155], v121 offset:4096
	v_mfma_f32_16x16x32_f16 v[34:37], v[180:183], v[204:207], v[34:37]
	ds_read_b128 v[156:159], v121 offset:6144
	v_mfma_f32_16x16x32_f16 v[30:33], v[184:187], v[192:195], v[30:33]
	ds_read_b128 v[160:163], v123
	v_mfma_f32_16x16x32_f16 v[26:29], v[184:187], v[196:199], v[26:29]
	ds_read_b128 v[164:167], v123 offset:2048
	v_mfma_f32_16x16x32_f16 v[22:25], v[184:187], v[200:203], v[22:25]
	ds_read_b128 v[168:171], v123 offset:4096
	v_mfma_f32_16x16x32_f16 v[18:21], v[184:187], v[204:207], v[18:21]
	ds_read_b128 v[172:175], v123 offset:6144
	v_mfma_f32_16x16x32_f16 v[14:17], v[188:191], v[192:195], v[14:17]
	v_mfma_f32_16x16x32_f16 v[10:13], v[188:191], v[196:199], v[10:13]
	s_mov_b32 m0, s49
	v_mfma_f32_16x16x32_f16 v[6:9], v[188:191], v[200:203], v[6:9]
	global_load_lds_dwordx4 v[76:77], off
	v_mfma_f32_16x16x32_f16 v[2:5], v[188:191], v[204:207], v[2:5]
	v_mfma_f32_16x16x32_f16 v[62:65], v[208:211], v[224:227], v[62:65]
	s_add_u32 m0, s49, 0x2000
	v_mfma_f32_16x16x32_f16 v[58:61], v[208:211], v[228:231], v[58:61]
	global_load_lds_dwordx4 v[74:75], off
	v_mfma_f32_16x16x32_f16 v[54:57], v[208:211], v[232:235], v[54:57]
	v_mfma_f32_16x16x32_f16 v[50:53], v[208:211], v[236:239], v[50:53]
	s_add_u32 m0, s49, 0x4000
	v_mfma_f32_16x16x32_f16 v[46:49], v[212:215], v[224:227], v[46:49]
	global_load_lds_dwordx4 v[70:71], off
	v_mfma_f32_16x16x32_f16 v[42:45], v[212:215], v[228:231], v[42:45]
	v_mfma_f32_16x16x32_f16 v[38:41], v[212:215], v[232:235], v[38:41]
	s_add_u32 m0, s49, 0x6000
	v_mfma_f32_16x16x32_f16 v[34:37], v[212:215], v[236:239], v[34:37]
	global_load_lds_dwordx4 v[68:69], off
	v_mfma_f32_16x16x32_f16 v[30:33], v[216:219], v[224:227], v[30:33]
	v_mfma_f32_16x16x32_f16 v[26:29], v[216:219], v[228:231], v[26:29]
	s_add_u32 m0, s49, 0x8000
	v_mfma_f32_16x16x32_f16 v[22:25], v[216:219], v[232:235], v[22:25]
	global_load_lds_dwordx4 v[72:73], off
	v_mfma_f32_16x16x32_f16 v[18:21], v[216:219], v[236:239], v[18:21]
	v_mfma_f32_16x16x32_f16 v[14:17], v[220:223], v[224:227], v[14:17]
	s_add_u32 m0, s49, 0xa000
	v_mfma_f32_16x16x32_f16 v[10:13], v[220:223], v[228:231], v[10:13]
	global_load_lds_dwordx4 v[66:67], off
	v_mfma_f32_16x16x32_f16 v[6:9], v[220:223], v[232:235], v[6:9]
	v_mfma_f32_16x16x32_f16 v[2:5], v[220:223], v[236:239], v[2:5]
	v_lshl_add_u64 v[76:77], v[76:77], 0, s[0:1]
	v_lshl_add_u64 v[74:75], v[74:75], 0, s[0:1]
	v_lshl_add_u64 v[70:71], v[70:71], 0, s[0:1]
	v_lshl_add_u64 v[68:69], v[68:69], 0, s[0:1]
	v_lshl_add_u64 v[72:73], v[72:73], 0, s[0:1]
	v_lshl_add_u64 v[66:67], v[66:67], 0, s[0:1]
	s_add_i32 s48, s48, 1
	s_add_i32 s49, s45, 1
	s_cmp_lg_u32 s45, 2
	s_cselect_b32 s45, s49, 0
	s_add_i32 s49, s46, 1
	s_cmp_lg_u32 s46, 2
	s_cselect_b32 s46, s49, 0
	s_cmp_lt_u32 s48, 12
	s_cbranch_scc1 .LBB1_36
	s_waitcnt vmcnt(6)
	s_waitcnt lgkmcnt(0)
	s_barrier
	s_mul_i32 s49, s46, 0xc000
	s_add_u32 s50, s49, s3
	s_add_u32 s51, s49, s2
	v_add3_u32 v120, s50, v86, v85
	v_add3_u32 v121, s50, v86, v84
	v_add3_u32 v122, s51, v81, v85
	v_add3_u32 v123, s51, v81, v84
	s_mul_i32 s49, s45, 0xc000
	s_add_u32 s49, s49, s44
	ds_read_b128 v[176:179], v120
	ds_read_b128 v[180:183], v120 offset:2048
	ds_read_b128 v[184:187], v120 offset:4096
	ds_read_b128 v[188:191], v120 offset:6144
	v_mfma_f32_16x16x32_f16 v[62:65], v[88:91], v[104:107], v[62:65]
	ds_read_b128 v[192:195], v122
	v_mfma_f32_16x16x32_f16 v[58:61], v[88:91], v[108:111], v[58:61]
	ds_read_b128 v[196:199], v122 offset:2048
	v_mfma_f32_16x16x32_f16 v[54:57], v[88:91], v[112:115], v[54:57]
	ds_read_b128 v[200:203], v122 offset:4096
	v_mfma_f32_16x16x32_f16 v[50:53], v[88:91], v[116:119], v[50:53]
	ds_read_b128 v[204:207], v122 offset:6144
	v_mfma_f32_16x16x32_f16 v[46:49], v[92:95], v[104:107], v[46:49]
	ds_read_b128 v[208:211], v121
	v_mfma_f32_16x16x32_f16 v[42:45], v[92:95], v[108:111], v[42:45]
	ds_read_b128 v[212:215], v121 offset:2048
	v_mfma_f32_16x16x32_f16 v[38:41], v[92:95], v[112:115], v[38:41]
	ds_read_b128 v[216:219], v121 offset:4096
	v_mfma_f32_16x16x32_f16 v[34:37], v[92:95], v[116:119], v[34:37]
	ds_read_b128 v[220:223], v121 offset:6144
	v_mfma_f32_16x16x32_f16 v[30:33], v[96:99], v[104:107], v[30:33]
	ds_read_b128 v[224:227], v123
	v_mfma_f32_16x16x32_f16 v[26:29], v[96:99], v[108:111], v[26:29]
	ds_read_b128 v[228:231], v123 offset:2048
	v_mfma_f32_16x16x32_f16 v[22:25], v[96:99], v[112:115], v[22:25]
	ds_read_b128 v[232:235], v123 offset:4096
	v_mfma_f32_16x16x32_f16 v[18:21], v[96:99], v[116:119], v[18:21]
	ds_read_b128 v[236:239], v123 offset:6144
	v_mfma_f32_16x16x32_f16 v[14:17], v[100:103], v[104:107], v[14:17]
	v_mfma_f32_16x16x32_f16 v[10:13], v[100:103], v[108:111], v[10:13]
	s_mov_b32 m0, s49
	v_mfma_f32_16x16x32_f16 v[6:9], v[100:103], v[112:115], v[6:9]
	global_load_lds_dwordx4 v[76:77], off
	v_mfma_f32_16x16x32_f16 v[2:5], v[100:103], v[116:119], v[2:5]
	v_mfma_f32_16x16x32_f16 v[62:65], v[144:147], v[160:163], v[62:65]
	s_add_u32 m0, s49, 0x2000
	v_mfma_f32_16x16x32_f16 v[58:61], v[144:147], v[164:167], v[58:61]
	global_load_lds_dwordx4 v[74:75], off
	v_mfma_f32_16x16x32_f16 v[54:57], v[144:147], v[168:171], v[54:57]
	v_mfma_f32_16x16x32_f16 v[50:53], v[144:147], v[172:175], v[50:53]
	s_add_u32 m0, s49, 0x4000
	v_mfma_f32_16x16x32_f16 v[46:49], v[148:151], v[160:163], v[46:49]
	global_load_lds_dwordx4 v[70:71], off
	v_mfma_f32_16x16x32_f16 v[42:45], v[148:151], v[164:167], v[42:45]
	v_mfma_f32_16x16x32_f16 v[38:41], v[148:151], v[168:171], v[38:41]
	s_add_u32 m0, s49, 0x6000
	v_mfma_f32_16x16x32_f16 v[34:37], v[148:151], v[172:175], v[34:37]
	global_load_lds_dwordx4 v[68:69], off
	v_mfma_f32_16x16x32_f16 v[30:33], v[152:155], v[160:163], v[30:33]
	v_mfma_f32_16x16x32_f16 v[26:29], v[152:155], v[164:167], v[26:29]
	s_add_u32 m0, s49, 0x8000
	v_mfma_f32_16x16x32_f16 v[22:25], v[152:155], v[168:171], v[22:25]
	global_load_lds_dwordx4 v[72:73], off
	v_mfma_f32_16x16x32_f16 v[18:21], v[152:155], v[172:175], v[18:21]
	v_mfma_f32_16x16x32_f16 v[14:17], v[156:159], v[160:163], v[14:17]
	s_add_u32 m0, s49, 0xa000
	v_mfma_f32_16x16x32_f16 v[10:13], v[156:159], v[164:167], v[10:13]
	global_load_lds_dwordx4 v[66:67], off
	v_mfma_f32_16x16x32_f16 v[6:9], v[156:159], v[168:171], v[6:9]
	v_mfma_f32_16x16x32_f16 v[2:5], v[156:159], v[172:175], v[2:5]
	v_lshl_add_u64 v[76:77], v[76:77], 0, s[0:1]
	v_lshl_add_u64 v[74:75], v[74:75], 0, s[0:1]
	v_lshl_add_u64 v[70:71], v[70:71], 0, s[0:1]
	v_lshl_add_u64 v[68:69], v[68:69], 0, s[0:1]
	v_lshl_add_u64 v[72:73], v[72:73], 0, s[0:1]
	v_lshl_add_u64 v[66:67], v[66:67], 0, s[0:1]
	s_add_i32 s48, s48, 1
	s_add_i32 s49, s45, 1
	s_cmp_lg_u32 s45, 2
	s_cselect_b32 s45, s49, 0
	s_add_i32 s49, s46, 1
	s_cmp_lg_u32 s46, 2
	s_cselect_b32 s46, s49, 0
	s_waitcnt vmcnt(6)
	s_waitcnt lgkmcnt(0)
	s_barrier
	s_mul_i32 s49, s46, 0xc000
	s_add_u32 s50, s49, s3
	s_add_u32 s51, s49, s2
	v_add3_u32 v120, s50, v86, v85
	v_add3_u32 v121, s50, v86, v84
	v_add3_u32 v122, s51, v81, v85
	v_add3_u32 v123, s51, v81, v84
	ds_read_b128 v[88:91], v120
	ds_read_b128 v[92:95], v120 offset:2048
	ds_read_b128 v[96:99], v120 offset:4096
	ds_read_b128 v[100:103], v120 offset:6144
	v_mfma_f32_16x16x32_f16 v[62:65], v[176:179], v[192:195], v[62:65]
	ds_read_b128 v[104:107], v122
	v_mfma_f32_16x16x32_f16 v[58:61], v[176:179], v[196:199], v[58:61]
	ds_read_b128 v[108:111], v122 offset:2048
	v_mfma_f32_16x16x32_f16 v[54:57], v[176:179], v[200:203], v[54:57]
	ds_read_b128 v[112:115], v122 offset:4096
	v_mfma_f32_16x16x32_f16 v[50:53], v[176:179], v[204:207], v[50:53]
	ds_read_b128 v[116:119], v122 offset:6144
	v_mfma_f32_16x16x32_f16 v[46:49], v[180:183], v[192:195], v[46:49]
	ds_read_b128 v[144:147], v121
	v_mfma_f32_16x16x32_f16 v[42:45], v[180:183], v[196:199], v[42:45]
	ds_read_b128 v[148:151], v121 offset:2048
	v_mfma_f32_16x16x32_f16 v[38:41], v[180:183], v[200:203], v[38:41]
	ds_read_b128 v[152:155], v121 offset:4096
	v_mfma_f32_16x16x32_f16 v[34:37], v[180:183], v[204:207], v[34:37]
	ds_read_b128 v[156:159], v121 offset:6144
	v_mfma_f32_16x16x32_f16 v[30:33], v[184:187], v[192:195], v[30:33]
	ds_read_b128 v[160:163], v123
	v_mfma_f32_16x16x32_f16 v[26:29], v[184:187], v[196:199], v[26:29]
	ds_read_b128 v[164:167], v123 offset:2048
	v_mfma_f32_16x16x32_f16 v[22:25], v[184:187], v[200:203], v[22:25]
	ds_read_b128 v[168:171], v123 offset:4096
	v_mfma_f32_16x16x32_f16 v[18:21], v[184:187], v[204:207], v[18:21]
	ds_read_b128 v[172:175], v123 offset:6144
	v_mfma_f32_16x16x32_f16 v[14:17], v[188:191], v[192:195], v[14:17]
	v_mfma_f32_16x16x32_f16 v[10:13], v[188:191], v[196:199], v[10:13]
	v_mfma_f32_16x16x32_f16 v[6:9], v[188:191], v[200:203], v[6:9]
	v_mfma_f32_16x16x32_f16 v[2:5], v[188:191], v[204:207], v[2:5]
	v_mfma_f32_16x16x32_f16 v[62:65], v[208:211], v[224:227], v[62:65]
	v_mfma_f32_16x16x32_f16 v[58:61], v[208:211], v[228:231], v[58:61]
	v_mfma_f32_16x16x32_f16 v[54:57], v[208:211], v[232:235], v[54:57]
	v_mfma_f32_16x16x32_f16 v[50:53], v[208:211], v[236:239], v[50:53]
	v_mfma_f32_16x16x32_f16 v[46:49], v[212:215], v[224:227], v[46:49]
	v_mfma_f32_16x16x32_f16 v[42:45], v[212:215], v[228:231], v[42:45]
	v_mfma_f32_16x16x32_f16 v[38:41], v[212:215], v[232:235], v[38:41]
	v_mfma_f32_16x16x32_f16 v[34:37], v[212:215], v[236:239], v[34:37]
	v_mfma_f32_16x16x32_f16 v[30:33], v[216:219], v[224:227], v[30:33]
	v_mfma_f32_16x16x32_f16 v[26:29], v[216:219], v[228:231], v[26:29]
	v_mfma_f32_16x16x32_f16 v[22:25], v[216:219], v[232:235], v[22:25]
	v_mfma_f32_16x16x32_f16 v[18:21], v[216:219], v[236:239], v[18:21]
	v_mfma_f32_16x16x32_f16 v[14:17], v[220:223], v[224:227], v[14:17]
	v_mfma_f32_16x16x32_f16 v[10:13], v[220:223], v[228:231], v[10:13]
	v_mfma_f32_16x16x32_f16 v[6:9], v[220:223], v[232:235], v[6:9]
	v_mfma_f32_16x16x32_f16 v[2:5], v[220:223], v[236:239], v[2:5]
	s_add_i32 s48, s48, 1
	s_add_i32 s49, s45, 1
	s_cmp_lg_u32 s45, 2
	s_cselect_b32 s45, s49, 0
	s_add_i32 s49, s46, 1
	s_cmp_lg_u32 s46, 2
	s_cselect_b32 s46, s49, 0
	s_waitcnt vmcnt(0)
	s_waitcnt lgkmcnt(0)
	s_barrier
	s_mul_i32 s49, s46, 0xc000
	s_add_u32 s50, s49, s3
	s_add_u32 s51, s49, s2
	v_add3_u32 v120, s50, v86, v85
	v_add3_u32 v121, s50, v86, v84
	v_add3_u32 v122, s51, v81, v85
	v_add3_u32 v123, s51, v81, v84
	ds_read_b128 v[176:179], v120
	ds_read_b128 v[180:183], v120 offset:2048
	ds_read_b128 v[184:187], v120 offset:4096
	ds_read_b128 v[188:191], v120 offset:6144
	v_mfma_f32_16x16x32_f16 v[62:65], v[88:91], v[104:107], v[62:65]
	ds_read_b128 v[192:195], v122
	v_mfma_f32_16x16x32_f16 v[58:61], v[88:91], v[108:111], v[58:61]
	ds_read_b128 v[196:199], v122 offset:2048
	v_mfma_f32_16x16x32_f16 v[54:57], v[88:91], v[112:115], v[54:57]
	ds_read_b128 v[200:203], v122 offset:4096
	v_mfma_f32_16x16x32_f16 v[50:53], v[88:91], v[116:119], v[50:53]
	ds_read_b128 v[204:207], v122 offset:6144
	v_mfma_f32_16x16x32_f16 v[46:49], v[92:95], v[104:107], v[46:49]
	ds_read_b128 v[208:211], v121
	v_mfma_f32_16x16x32_f16 v[42:45], v[92:95], v[108:111], v[42:45]
	ds_read_b128 v[212:215], v121 offset:2048
	v_mfma_f32_16x16x32_f16 v[38:41], v[92:95], v[112:115], v[38:41]
	ds_read_b128 v[216:219], v121 offset:4096
	v_mfma_f32_16x16x32_f16 v[34:37], v[92:95], v[116:119], v[34:37]
	ds_read_b128 v[220:223], v121 offset:6144
	v_mfma_f32_16x16x32_f16 v[30:33], v[96:99], v[104:107], v[30:33]
	ds_read_b128 v[224:227], v123
	v_mfma_f32_16x16x32_f16 v[26:29], v[96:99], v[108:111], v[26:29]
	ds_read_b128 v[228:231], v123 offset:2048
	v_mfma_f32_16x16x32_f16 v[22:25], v[96:99], v[112:115], v[22:25]
	ds_read_b128 v[232:235], v123 offset:4096
	v_mfma_f32_16x16x32_f16 v[18:21], v[96:99], v[116:119], v[18:21]
	ds_read_b128 v[236:239], v123 offset:6144
	v_mfma_f32_16x16x32_f16 v[14:17], v[100:103], v[104:107], v[14:17]
	v_mfma_f32_16x16x32_f16 v[10:13], v[100:103], v[108:111], v[10:13]
	v_mfma_f32_16x16x32_f16 v[6:9], v[100:103], v[112:115], v[6:9]
	v_mfma_f32_16x16x32_f16 v[2:5], v[100:103], v[116:119], v[2:5]
	v_mfma_f32_16x16x32_f16 v[62:65], v[144:147], v[160:163], v[62:65]
	v_mfma_f32_16x16x32_f16 v[58:61], v[144:147], v[164:167], v[58:61]
	v_mfma_f32_16x16x32_f16 v[54:57], v[144:147], v[168:171], v[54:57]
	v_mfma_f32_16x16x32_f16 v[50:53], v[144:147], v[172:175], v[50:53]
	v_mfma_f32_16x16x32_f16 v[46:49], v[148:151], v[160:163], v[46:49]
	v_mfma_f32_16x16x32_f16 v[42:45], v[148:151], v[164:167], v[42:45]
	v_mfma_f32_16x16x32_f16 v[38:41], v[148:151], v[168:171], v[38:41]
	v_mfma_f32_16x16x32_f16 v[34:37], v[148:151], v[172:175], v[34:37]
	v_mfma_f32_16x16x32_f16 v[30:33], v[152:155], v[160:163], v[30:33]
	v_mfma_f32_16x16x32_f16 v[26:29], v[152:155], v[164:167], v[26:29]
	v_mfma_f32_16x16x32_f16 v[22:25], v[152:155], v[168:171], v[22:25]
	v_mfma_f32_16x16x32_f16 v[18:21], v[152:155], v[172:175], v[18:21]
	v_mfma_f32_16x16x32_f16 v[14:17], v[156:159], v[160:163], v[14:17]
	v_mfma_f32_16x16x32_f16 v[10:13], v[156:159], v[164:167], v[10:13]
	v_mfma_f32_16x16x32_f16 v[6:9], v[156:159], v[168:171], v[6:9]
	v_mfma_f32_16x16x32_f16 v[2:5], v[156:159], v[172:175], v[2:5]
	s_add_i32 s48, s48, 1
	s_add_i32 s49, s45, 1
	s_cmp_lg_u32 s45, 2
	s_cselect_b32 s45, s49, 0
	s_add_i32 s49, s46, 1
	s_cmp_lg_u32 s46, 2
	s_cselect_b32 s46, s49, 0
	s_waitcnt lgkmcnt(0)
	v_mfma_f32_16x16x32_f16 v[62:65], v[176:179], v[192:195], v[62:65]
	v_mfma_f32_16x16x32_f16 v[58:61], v[176:179], v[196:199], v[58:61]
	v_mfma_f32_16x16x32_f16 v[54:57], v[176:179], v[200:203], v[54:57]
	v_mfma_f32_16x16x32_f16 v[50:53], v[176:179], v[204:207], v[50:53]
	v_mfma_f32_16x16x32_f16 v[46:49], v[180:183], v[192:195], v[46:49]
	v_mfma_f32_16x16x32_f16 v[42:45], v[180:183], v[196:199], v[42:45]
	v_mfma_f32_16x16x32_f16 v[38:41], v[180:183], v[200:203], v[38:41]
	v_mfma_f32_16x16x32_f16 v[34:37], v[180:183], v[204:207], v[34:37]
	v_mfma_f32_16x16x32_f16 v[30:33], v[184:187], v[192:195], v[30:33]
	v_mfma_f32_16x16x32_f16 v[26:29], v[184:187], v[196:199], v[26:29]
	v_mfma_f32_16x16x32_f16 v[22:25], v[184:187], v[200:203], v[22:25]
	v_mfma_f32_16x16x32_f16 v[18:21], v[184:187], v[204:207], v[18:21]
	v_mfma_f32_16x16x32_f16 v[14:17], v[188:191], v[192:195], v[14:17]
	v_mfma_f32_16x16x32_f16 v[10:13], v[188:191], v[196:199], v[10:13]
	v_mfma_f32_16x16x32_f16 v[6:9], v[188:191], v[200:203], v[6:9]
	v_mfma_f32_16x16x32_f16 v[2:5], v[188:191], v[204:207], v[2:5]
	v_mfma_f32_16x16x32_f16 v[62:65], v[208:211], v[224:227], v[62:65]
	v_mfma_f32_16x16x32_f16 v[58:61], v[208:211], v[228:231], v[58:61]
	v_mfma_f32_16x16x32_f16 v[54:57], v[208:211], v[232:235], v[54:57]
	v_mfma_f32_16x16x32_f16 v[50:53], v[208:211], v[236:239], v[50:53]
	v_mfma_f32_16x16x32_f16 v[46:49], v[212:215], v[224:227], v[46:49]
	v_mfma_f32_16x16x32_f16 v[42:45], v[212:215], v[228:231], v[42:45]
	v_mfma_f32_16x16x32_f16 v[38:41], v[212:215], v[232:235], v[38:41]
	v_mfma_f32_16x16x32_f16 v[34:37], v[212:215], v[236:239], v[34:37]
	v_mfma_f32_16x16x32_f16 v[30:33], v[216:219], v[224:227], v[30:33]
	v_mfma_f32_16x16x32_f16 v[26:29], v[216:219], v[228:231], v[26:29]
	v_mfma_f32_16x16x32_f16 v[22:25], v[216:219], v[232:235], v[22:25]
	v_mfma_f32_16x16x32_f16 v[18:21], v[216:219], v[236:239], v[18:21]
	v_mfma_f32_16x16x32_f16 v[14:17], v[220:223], v[224:227], v[14:17]
	v_mfma_f32_16x16x32_f16 v[10:13], v[220:223], v[228:231], v[10:13]
	v_mfma_f32_16x16x32_f16 v[6:9], v[220:223], v[232:235], v[6:9]
	v_mfma_f32_16x16x32_f16 v[2:5], v[220:223], v[236:239], v[2:5]
	s_setprio 0
	s_branch .Lqk_epi_start
